# v13 + one static s_setprio 1 for waves 4-7 (younger half) before the k3 main loop
# speedup vs baseline: 1.0581x; 1.0581x over previous
.LBB2_414:
	s_movk_i32 s0, 0xc00
	v_mov_b64_e32 v[26:27], s[42:43]
	v_mul_u32_u24_e32 v28, 0xc00, v154
	v_mad_i64_i32 v[26:27], s[0:1], v62, s0, v[26:27]
	v_or_b32_e32 v28, v28, v98
	v_mov_b32_e32 v99, 0
	v_lshl_add_u64 v[26:27], v[26:27], 0, v[98:99]
	v_or_b32_e32 v29, 0x10000, v28
	global_store_dwordx4 v[26:27], v[22:25], off sc1
	ds_write_b128 v29, v[22:25]
	v_sub_f32_e32 v10, v10, v22
	v_or_b32_e32 v22, v101, v154
	v_sub_f32_e32 v11, v11, v23
	v_add_u32_e32 v23, v22, v102
	v_lshl_or_b32 v23, v23, 4, v103
	ds_write_b32 v23, v10
	v_add_u32_e32 v10, v22, v104
	v_lshl_or_b32 v10, v10, 4, v105
	ds_write_b32 v10, v11
	v_or_b32_e32 v10, v106, v154
	v_add_u32_e32 v10, v10, v107
	v_sub_f32_e32 v12, v12, v24
	v_lshl_or_b32 v10, v10, 4, v108
	ds_write_b32 v10, v12
	v_or_b32_e32 v10, v109, v154
	v_add_u32_e32 v10, v10, v110
	v_sub_f32_e32 v13, v13, v25
	v_lshl_or_b32 v10, v10, 4, v111
	ds_write_b32 v10, v13
	v_add_u32_e32 v10, 0x10400, v28
	ds_write_b128 v10, v[18:21]
	v_sub_f32_e32 v10, v6, v18
	v_sub_f32_e32 v11, v7, v19
	v_pk_add_f32 v[6:7], v[8:9], v[20:21] neg_lo:[0,1] neg_hi:[0,1]
	v_or_b32_e32 v8, v112, v154
	v_add_u32_e32 v9, v8, v113
	v_add_u32_e32 v8, v8, v115
	v_lshl_or_b32 v9, v9, 4, v114
	v_lshl_or_b32 v8, v8, 4, v116
	ds_write_b32 v9, v10
	ds_write_b32 v8, v11
	v_or_b32_e32 v8, v117, v154
	v_add_u32_e32 v8, v8, v118
	v_lshl_or_b32 v8, v8, 4, v119
	ds_write_b32 v8, v6
	v_or_b32_e32 v6, v120, v154
	v_add_u32_e32 v6, v6, v121
	v_lshl_or_b32 v6, v6, 4, v122
	ds_write_b32 v6, v7
	v_add_u32_e32 v6, 0x10800, v28
	ds_write_b128 v6, v[14:17]
	v_or_b32_e32 v6, v123, v154
	v_add_u32_e32 v7, v6, v124
	v_pk_add_f32 v[2:3], v[2:3], v[14:15] neg_lo:[0,1] neg_hi:[0,1]
	v_lshl_or_b32 v7, v7, 4, v125
	ds_write_b32 v7, v2
	v_add_u32_e32 v2, v6, v126
	v_lshl_or_b32 v2, v2, 4, v127
	ds_write_b32 v2, v3
	v_or_b32_e32 v2, v133, v154
	v_add_u32_e32 v2, v2, v134
	v_pk_add_f32 v[4:5], v[4:5], v[16:17] neg_lo:[0,1] neg_hi:[0,1]
	v_lshl_or_b32 v2, v2, 4, v63
	ds_write_b32 v2, v4
	v_or_b32_e32 v2, v135, v154
	v_add_u32_e32 v2, v2, v132
	v_lshl_or_b32 v2, v2, 4, v136
	v_add_lshl_u32 v4, v100, v154, 4
	s_mov_b32 s5, 0
	s_mov_b32 s4, 1.0
	ds_write_b32 v2, v5
	v_mov_b64_e32 v[2:3], s[4:5]
	v_add_u32_e32 v4, 8, v4
	s_waitcnt vmcnt(1)
	v_lshlrev_b32_e32 v40, 9, v150
	ds_write2st64_b64 v4, v[2:3], v[2:3] offset1:64
	v_or_b32_e32 v2, v40, v128
	v_lshlrev_b32_e32 v98, 4, v2
	v_lshl_add_u64 v[100:101], s[40:41], 0, v[98:99]
	s_mov_b64 s[0:1], 0x787000
	v_lshl_add_u64 v[34:35], v[100:101], 0, s[0:1]
	s_mov_b32 s0, 0x788000
	v_add_co_u32_e32 v36, vcc, s0, v100
	global_store_dwordx4 v[26:27], v[18:21], off offset:1024 sc1
	global_store_dwordx4 v[26:27], v[14:17], off offset:2048 sc1
	s_lshr_b32 s59, s33, 4
	s_and_b32 s59, s59, 31
	s_lshl_b32 s59, s59, 15
	s_add_u32 s59, s59, 0x787000
	s_add_u32 s68, s40, s59
	s_addc_u32 s69, s41, 0
	v_lshlrev_b32_e32 v207, 6, v0
	global_load_dword v207, v207, s[68:69]
	s_waitcnt lgkmcnt(0)
	s_barrier
	v_addc_co_u32_e32 v37, vcc, 0, v101, vcc
	global_load_dwordx4 v[2:5], v[34:35], off offset:1024
	global_load_dwordx4 v[10:13], v[34:35], off offset:2048
	global_load_dwordx4 v[14:17], v[34:35], off offset:3072
	global_load_dwordx4 v[6:9], v[36:37], off offset:-4096
	global_load_dwordx4 v[18:21], v[36:37], off
	global_load_dwordx4 v[22:25], v[36:37], off offset:1024
	global_load_dwordx4 v[26:29], v[36:37], off offset:2048
	global_load_dwordx4 v[30:33], v[36:37], off offset:3072
	v_and_b32_e32 v35, 15, v0
	v_lshrrev_b32_e32 v37, 4, v128
	v_lshlrev_b32_e32 v102, 2, v35
	v_lshlrev_b32_e32 v41, 2, v37
	v_lshlrev_b32_e32 v34, 4, v35
	v_cmp_gt_u32_e64 s[0:1], 6, v35
	v_mov_b32_e32 v35, v99
	v_or3_b32 v36, v34, v41, v40
	v_lshl_add_u64 v[104:105], s[44:45], 0, v[34:35]
	v_or_b32_e32 v34, v40, v34
	s_movk_i32 s4, 0x1000
	v_or3_b32 v153, v34, v41, s4
	v_or_b32_e32 v34, 0x11800, v98
	v_lshl_add_u64 v[118:119], s[40:41], 0, v[34:35]
	v_or_b32_e32 v34, 0x11400, v98
	v_lshl_add_u64 v[120:121], s[40:41], 0, v[34:35]
	v_or_b32_e32 v34, 0x11000, v98
	ds_read2st64_b32 v[132:133], v36 offset1:1
	v_or_b32_e32 v36, s33, v41
	v_lshl_add_u64 v[122:123], s[40:41], 0, v[34:35]
	v_or_b32_e32 v34, 0x10c00, v98
	v_or_b32_e32 v38, 1, v36
	v_lshl_add_u64 v[124:125], s[40:41], 0, v[34:35]
	v_or_b32_e32 v34, 0x10800, v98
	v_mul_u32_u24_e32 v152, 0x3000, v37
	v_ashrrev_i32_e32 v37, 31, v36
	v_ashrrev_i32_e32 v39, 31, v38
	v_lshl_add_u64 v[126:127], s[40:41], 0, v[34:35]
	v_or_b32_e32 v34, 0x10400, v98
	v_mov_b32_e32 v103, v99
	v_lshlrev_b64 v[108:109], 17, v[36:37]
	v_lshlrev_b64 v[110:111], 17, v[38:39]
	v_or_b32_e32 v38, 2, v36
	v_or_b32_e32 v36, 3, v36
	v_lshl_add_u64 v[128:129], s[40:41], 0, v[34:35]
	v_mul_u32_u24_e32 v34, 24, v150
	v_lshl_add_u64 v[106:107], s[38:39], 0, v[102:103]
	v_ashrrev_i32_e32 v39, 31, v38
	v_ashrrev_i32_e32 v37, 31, v36
	v_lshlrev_b32_e32 v103, 2, v0
	v_or_b32_e32 v98, 0x11c00, v98
	v_or_b32_e32 v34, v152, v34
	v_lshlrev_b64 v[112:113], 17, v[38:39]
	v_lshlrev_b64 v[114:115], 17, v[36:37]
	v_and_b32_e32 v116, 0x700, v103
	v_mov_b32_e32 v117, v99
	v_lshl_add_u64 v[130:131], s[40:41], 0, v[98:99]
	v_add_u32_e32 v154, v34, v102
	s_mov_b64 s[6:7], 0
	s_mov_b64 s[8:9], 0x800
	v_mov_b32_e32 v155, 0x400
	v_mov_b32_e32 v159, 0
	v_mov_b32_e32 v158, 0
	v_mov_b32_e32 v157, 0
	v_mov_b32_e32 v156, 0
	v_readfirstlane_b32 s78, v150
	v_and_b32_e32 v104, 63, v0
	v_lshlrev_b32_e32 v104, 4, v104
	v_lshl_or_b32 v104, v150, 13, v104
	v_add_u32_e32 v105, 0xfffff000, v153
	v_mov_b32_e32 v106, v154
	v_lshrrev_b32_e32 v98, 2, v102
	v_cmp_gt_u32_e32 vcc, 6, v98
	v_add_u32_e32 v107, -6, v98
	s_nop 0
	v_cndmask_b32_e32 v107, v107, v98, vcc
	v_cmp_gt_u32_e32 vcc, 6, v107
	v_add_u32_e32 v98, -6, v107
	s_nop 0
	v_cndmask_b32_e32 v107, v98, v107, vcc
	v_lshlrev_b32_e32 v107, 2, v107
	v_sub_u32_e32 v106, v106, v102
	v_add_u32_e32 v106, v106, v107
	v_and_b32_e32 v98, 63, v0
	v_lshrrev_b32_e32 v98, 4, v98
	v_lshlrev_b32_e32 v98, 19, v98
	v_lshl_or_b32 v108, v102, 2, v98
	v_add_u32_e32 v109, 0x20000, v108
	v_add_u32_e32 v110, 0x40000, v108
	v_add_u32_e32 v111, 0x60000, v108
	v_mov_b32_e32 v240, 0
	v_mov_b32_e32 v241, 0
	v_mov_b32_e32 v242, 0
	v_mov_b32_e32 v243, 0
	s_cmp_lt_u32 s78, 4
	s_cbranch_scc1 .Lk3m_noprio
	s_setprio 1
.Lk3m_noprio:
	s_nop 0
	s_lshl_b32 s84, s33, 17
	s_lshl_b32 s85, s78, 10
	s_add_u32 s84, s84, s85
	s_add_u32 s80, s44, s84
	s_addc_u32 s81, s45, 0
	s_mul_i32 s84, s78, 0x1800
	s_add_u32 s94, s38, s84
	s_addc_u32 s95, s39, 0
	s_mov_b32 s70, 0
	s_add_u32 s86, s40, 0x797000
	s_addc_u32 s87, s41, 0
	s_add_u32 s88, s86, 0x1000
	s_addc_u32 s89, s87, 0
	v_add_u32_e32 v112, 0x1000, v105
	s_waitcnt vmcnt(0) lgkmcnt(0)
	v_mfma_f32_16x16x4_f32 v[34:37], v132, v6, 0
	v_mfma_f32_16x16x4_f32 v[38:41], v132, v8, 0
	v_mfma_f32_16x16x4_f32 v[34:37], v133, v7, v[34:37]
	v_mfma_f32_16x16x4_f32 v[38:41], v133, v9, v[38:41]
	global_load_dwordx4 v[6:9], v104, s[86:87]
	v_mfma_f32_16x16x4_f32 v[42:45], v132, v2, 0
	v_mfma_f32_16x16x4_f32 v[46:49], v132, v4, 0
	v_mfma_f32_16x16x4_f32 v[42:45], v133, v3, v[42:45]
	v_mfma_f32_16x16x4_f32 v[46:49], v133, v5, v[46:49]
	global_load_dwordx4 v[2:5], v104, s[86:87] offset:1024
	v_mfma_f32_16x16x4_f32 v[50:53], v132, v10, 0
	v_mfma_f32_16x16x4_f32 v[54:57], v132, v12, 0
	v_mfma_f32_16x16x4_f32 v[50:53], v133, v11, v[50:53]
	v_mfma_f32_16x16x4_f32 v[54:57], v133, v13, v[54:57]
	global_load_dwordx4 v[10:13], v104, s[86:87] offset:2048
	v_mfma_f32_16x16x4_f32 v[58:61], v132, v14, 0
	v_mfma_f32_16x16x4_f32 v[62:65], v132, v16, 0
	v_mfma_f32_16x16x4_f32 v[58:61], v133, v15, v[58:61]
	v_mfma_f32_16x16x4_f32 v[62:65], v133, v17, v[62:65]
	global_load_dwordx4 v[14:17], v104, s[86:87] offset:3072
	v_mfma_f32_16x16x4_f32 v[66:69], v132, v18, 0
	v_mfma_f32_16x16x4_f32 v[70:73], v132, v20, 0
	v_mfma_f32_16x16x4_f32 v[66:69], v133, v19, v[66:69]
	v_mfma_f32_16x16x4_f32 v[70:73], v133, v21, v[70:73]
	global_load_dwordx4 v[18:21], v104, s[88:89]
	v_mfma_f32_16x16x4_f32 v[74:77], v132, v22, 0
	v_mfma_f32_16x16x4_f32 v[78:81], v132, v24, 0
	v_mfma_f32_16x16x4_f32 v[74:77], v133, v23, v[74:77]
	v_mfma_f32_16x16x4_f32 v[78:81], v133, v25, v[78:81]
	global_load_dwordx4 v[22:25], v104, s[88:89] offset:1024
	v_mfma_f32_16x16x4_f32 v[82:85], v132, v26, 0
	v_mfma_f32_16x16x4_f32 v[86:89], v132, v28, 0
	v_mfma_f32_16x16x4_f32 v[82:85], v133, v27, v[82:85]
	v_mfma_f32_16x16x4_f32 v[86:89], v133, v29, v[86:89]
	global_load_dwordx4 v[26:29], v104, s[88:89] offset:2048
	v_mfma_f32_16x16x4_f32 v[90:93], v132, v30, 0
	v_mfma_f32_16x16x4_f32 v[94:97], v132, v32, 0
	v_mfma_f32_16x16x4_f32 v[90:93], v133, v31, v[90:93]
	v_mfma_f32_16x16x4_f32 v[94:97], v133, v33, v[94:97]
	global_load_dwordx4 v[30:33], v104, s[88:89] offset:3072
	ds_read2st64_b32 v[132:133], v112 offset1:1
	s_nop 7
	s_nop 7
	v_max3_f32 v114, v34, v38, v42
	v_max3_f32 v116, v46, v50, v54
	v_max3_f32 v114, v114, v58, v62
	v_max3_f32 v116, v116, v66, v70
	v_max3_f32 v114, v114, v74, v78
	v_max3_f32 v116, v116, v82, v86
	v_max3_f32 v114, v114, v90, v94
	v_max_f32_e32 v114, v114, v116
	s_nop 1
	v_max_f32_dpp v114, v114, v114 row_ror:1 row_mask:0xf bank_mask:0xf
	s_nop 1
	v_max_f32_dpp v114, v114, v114 row_ror:2 row_mask:0xf bank_mask:0xf
	s_nop 1
	v_max_f32_dpp v114, v114, v114 row_ror:4 row_mask:0xf bank_mask:0xf
	s_nop 1
	v_max_f32_dpp v114, v114, v114 row_ror:8 row_mask:0xf bank_mask:0xf
	s_waitcnt vmcnt(0) lgkmcnt(0)
